# GQA loop: second-group PV fragment reads issued in the last QK gaps
# speedup vs baseline: 1.0103x; 1.0097x over previous
; __device__ __forceinline__ void finishSM(f32x16& p0, f32x16& p1, float alpha, float& l_reg, bf16x8& pa0, bf16x8& pa1, bf16x8& pa2, bf16x8& pa3) {
; #pragma unroll
;     for (int r = 0; r < 16; ++r) p1[r] = EXP_PROBE ? fmaf(p1[r], 0.001f, 1.f) : __builtin_amdgcn_exp2f(p1[r]);
;     float ps = 0.f;
; #pragma unroll
;     for (int r = 0; r < 16; ++r) ps += p0[r];
; #pragma unroll
;     for (int r = 0; r < 16; ++r) ps += p1[r];
;     { auto rr = __builtin_amdgcn_permlane32_swap(__float_as_uint(ps), __float_as_uint(ps), false, false);
;       ps = __uint_as_float(rr[0]) + __uint_as_float(rr[1]); }
;     l_reg = l_reg * alpha + ps;
;     ATT_PKN(p0, 0, pa0); ATT_PKN(p0, 8, pa1); ATT_PKN(p1, 0, pa2); ATT_PKN(p1, 8, pa3);
; }
; template <int DQK> __device__ __forceinline__ void qkt(f32x16& p0, f32x16& p1, const LAS char* buf, const bf16x8* qr, int r32, int hi, const f32x16& negm) {
; #pragma unroll
;     for (int d0 = 0; d0 < 4; ++d0) { const int ch = d0 * 2 + hi;
;         const bf16x8 b0 = *(const LAS bf16x8*)(buf + B_KN + swz64(r32, ch));
;         const bf16x8 b1 = *(const LAS bf16x8*)(buf + B_KN + swz64(32 + r32, ch));
;         p0 = __builtin_amdgcn_mfma_f32_32x32x16_bf16(b0, qr[d0], d0 == 0 ? negm : p0, 0, 0, 0);
;         p1 = __builtin_amdgcn_mfma_f32_32x32x16_bf16(b1, qr[d0], d0 == 0 ? negm : p1, 0, 0, 0); }
;     if constexpr (DQK == 96) {
; #pragma unroll
;         for (int d0 = 0; d0 < 2; ++d0) { const int ch = d0 * 2 + hi;
;             const bf16x8 b0 = *(const LAS bf16x8*)(buf + B_KR + swz32(r32, ch));
;             const bf16x8 b1 = *(const LAS bf16x8*)(buf + B_KR + swz32(32 + r32, ch));
;             p0 = __builtin_amdgcn_mfma_f32_32x32x16_bf16(b0, qr[4 + d0], p0, 0, 0, 0);
;             p1 = __builtin_amdgcn_mfma_f32_32x32x16_bf16(b1, qr[4 + d0], p1, 0, 0, 0); }
;     }
; }
; template <int D0> __device__ __forceinline__ void pv_one(f32x16& od, unsigned vb, bf16x8 pa0, bf16x8 pa1, bf16x8 pa2, bf16x8 pa3) {
;     const s16x4 l0 = tr_read<v_rd_off(D0, 0, 0)>(vb), h0 = tr_read<v_rd_off(D0, 0, 1)>(vb), l1 = tr_read<v_rd_off(D0, 1, 0)>(vb), h1 = tr_read<v_rd_off(D0, 1, 1)>(vb);
;     const s16x4 l2 = tr_read<v_rd_off(D0, 2, 0)>(vb), h2 = tr_read<v_rd_off(D0, 2, 1)>(vb), l3 = tr_read<v_rd_off(D0, 3, 0)>(vb), h3 = tr_read<v_rd_off(D0, 3, 1)>(vb);
;     asm volatile("s_waitcnt lgkmcnt(0)" ::: "memory"); SBAR();
.LBB0_497:
	s_mov_b32 s1, s11
	s_mov_b32 s11, s35
	s_waitcnt lgkmcnt(0)
	s_barrier
	v_add_u32_e32 v252, s1, v208
	v_add_u32_e32 v228, v252, v209
	ds_read_b128 v[224:227], v228
	ds_read_b128 v[228:231], v228 offset:4096
	v_add_u32_e32 v236, v252, v210
	ds_read_b128 v[232:235], v236
	ds_read_b128 v[236:239], v236 offset:4096
	v_add_u32_e32 v244, v252, v211
	ds_read_b128 v[240:243], v244
	ds_read_b128 v[244:247], v244 offset:4096
	v_add_u32_e32 v253, v252, v212
	ds_read_b128 v[248:251], v253
	v_exp_f32_e32 v66, v66
	v_exp_f32_e32 v67, v67
	v_exp_f32_e32 v68, v68
	v_exp_f32_e32 v69, v69
	v_exp_f32_e32 v70, v70
	v_exp_f32_e32 v71, v71
	v_exp_f32_e32 v72, v72
	v_exp_f32_e32 v73, v73
	s_waitcnt lgkmcnt(6)
	v_mfma_f32_32x32x16_bf16 v[98:113], v[224:227], v[114:117], v[18:33]
	ds_read_b128 v[224:227], v253 offset:4096
	v_exp_f32_e32 v74, v74
	v_exp_f32_e32 v75, v75
	v_exp_f32_e32 v76, v76
	v_cvt_pk_bf16_f32 v156, v143, v145
	v_cvt_pk_bf16_f32 v157, v141, v144
	v_add_f32_e32 v164, 0, v143
	v_add_f32_e32 v164, v145, v164
	v_add_f32_e32 v164, v141, v164
	s_waitcnt lgkmcnt(6)
	v_mfma_f32_32x32x16_bf16 v[82:97], v[228:231], v[114:117], v[18:33]
	v_exp_f32_e32 v77, v77
	v_exp_f32_e32 v78, v78
	v_exp_f32_e32 v79, v79
	v_cvt_pk_bf16_f32 v158, v139, v142
	v_cvt_pk_bf16_f32 v159, v138, v140
	v_add_f32_e32 v164, v144, v164
	v_add_f32_e32 v164, v139, v164
	v_add_f32_e32 v164, v142, v164
	s_waitcnt lgkmcnt(5)
	v_mfma_f32_32x32x16_bf16 v[98:113], v[232:235], v[12:15], v[98:113]
	v_exp_f32_e32 v80, v80
	v_exp_f32_e32 v81, v81
	v_cvt_pk_bf16_f32 v160, v151, v153
	v_cvt_pk_bf16_f32 v161, v149, v152
	v_cvt_pk_bf16_f32 v162, v147, v150
	v_cvt_pk_bf16_f32 v163, v146, v148
	v_add_f32_e32 v164, v138, v164
	v_add_f32_e32 v164, v140, v164
	v_add_f32_e32 v164, v151, v164
	s_waitcnt lgkmcnt(4)
	v_mfma_f32_32x32x16_bf16 v[82:97], v[236:239], v[12:15], v[82:97]
	v_add_f32_e32 v164, v153, v164
	v_add_f32_e32 v164, v149, v164
	v_add_f32_e32 v164, v152, v164
	v_add_f32_e32 v164, v147, v164
	v_add_f32_e32 v164, v150, v164
	v_add_f32_e32 v164, v146, v164
	v_add_f32_e32 v164, v148, v164
	s_waitcnt lgkmcnt(3)
	v_mfma_f32_32x32x16_bf16 v[98:113], v[240:243], v[8:11], v[98:113]
	v_add_u32_e32 v2, s11, v213
	ds_read_b64_tr_b16 v[138:139], v2 offset:0
	ds_read_b64_tr_b16 v[140:141], v2 offset:1024
	ds_read_b64_tr_b16 v[142:143], v2 offset:2048
	ds_read_b64_tr_b16 v[144:145], v2 offset:3072
	v_add_f32_e32 v164, v66, v164
	v_add_f32_e32 v164, v67, v164
	v_add_f32_e32 v164, v68, v164
	v_add_f32_e32 v164, v69, v164
	s_waitcnt lgkmcnt(6)
	v_mfma_f32_32x32x16_bf16 v[82:97], v[244:247], v[8:11], v[82:97]
	ds_read_b64_tr_b16 v[146:147], v2 offset:4096
	ds_read_b64_tr_b16 v[148:149], v2 offset:5120
	ds_read_b64_tr_b16 v[150:151], v2 offset:6144
	ds_read_b64_tr_b16 v[152:153], v2 offset:7168
	v_add_f32_e32 v164, v70, v164
	v_add_f32_e32 v164, v71, v164
	v_add_f32_e32 v164, v72, v164
	v_add_f32_e32 v164, v73, v164
	s_waitcnt lgkmcnt(9)
	v_mfma_f32_32x32x16_bf16 v[98:113], v[248:251], v[4:7], v[98:113]
	v_add_f32_e32 v164, v74, v164
	v_add_f32_e32 v164, v75, v164
	v_add_f32_e32 v164, v76, v164
	v_add_f32_e32 v164, v77, v164
	ds_read_b64_tr_b16 v[228:229], v2 offset:2560
	ds_read_b64_tr_b16 v[230:231], v2 offset:3584
	ds_read_b64_tr_b16 v[232:233], v2 offset:4608
	s_waitcnt lgkmcnt(11)
	v_mfma_f32_32x32x16_bf16 v[82:97], v[224:227], v[4:7], v[82:97]
	ds_read_b64_tr_b16 v[234:235], v2 offset:5632
	ds_read_b64_tr_b16 v[236:237], v2 offset:6656
	ds_read_b64_tr_b16 v[238:239], v2 offset:7680
	ds_read_b64_tr_b16 v[224:225], v2 offset:512
	ds_read_b64_tr_b16 v[226:227], v2 offset:1536
	s_waitcnt lgkmcnt(8)
	v_mfma_f32_32x32x16_bf16 v[50:65], v[138:141], v[156:159], v[50:65]
	v_add_f32_e32 v164, v78, v164
	v_add_f32_e32 v164, v79, v164
	v_add_f32_e32 v164, v80, v164
	v_add_f32_e32 v154, v81, v164
	v_mov_b32_e32 v155, v154
	v_mfma_f32_32x32x16_bf16 v[50:65], v[142:145], v[160:163], v[50:65]
	v_cvt_pk_bf16_f32 v66, v66, v67
	v_cvt_pk_bf16_f32 v67, v68, v69
	v_cvt_pk_bf16_f32 v68, v70, v71
	v_cvt_pk_bf16_f32 v69, v72, v73
	v_cvt_pk_bf16_f32 v70, v74, v75
	v_cvt_pk_bf16_f32 v71, v76, v77
	v_cvt_pk_bf16_f32 v72, v78, v79
	v_cvt_pk_bf16_f32 v73, v80, v81
	v_permlane32_swap_b32_e32 v154, v155
	v_mfma_f32_32x32x16_bf16 v[50:65], v[146:149], v[66:69], v[50:65]
	s_add_i32 s8, s13, -1
	s_cmp_lt_u32 s8, s31
	s_cselect_b32 s9, 0, s31
	s_cselect_b32 s35, s12, s29
	s_lshl_b32 s9, s9, 6
	s_sub_i32 s9, s35, s9
	v_add_u32_e32 v252, s9, v137
	v_subrev_u32_e32 v126, 64, v252
	v_ashrrev_i32_e32 v127, 31, v126
	v_mfma_f32_32x32x16_bf16 v[50:65], v[150:153], v[70:73], v[50:65]
	v_lshlrev_b64 v[126:127], 8, v[126:127]
	v_lshl_add_u64 v[128:129], v[16:17], 0, v[126:127]
	v_lshl_add_u64 v[126:127], v[134:135], 0, v[126:127]
	global_load_dwordx4 v[130:133], v[128:129], off
	s_nop 0
	global_load_dwordx4 v[126:129], v[126:127], off
	s_waitcnt lgkmcnt(0)
	v_mfma_f32_32x32x16_bf16 v[34:49], v[224:227], v[156:159], v[34:49]
	s_waitcnt vmcnt(2)
	v_add_u32_e32 v165, s10, v187
	ds_write_b128 v165, v[118:121]
	v_add_u32_e32 v165, s10, v214
	ds_write_b128 v165, v[122:125] offset:12288
	v_exp_f32_e32 v168, v98
	v_exp_f32_e32 v169, v99
	v_mfma_f32_32x32x16_bf16 v[34:49], v[228:231], v[160:163], v[34:49]
	v_exp_f32_e32 v170, v100
	v_exp_f32_e32 v171, v101
	v_exp_f32_e32 v172, v102
	v_exp_f32_e32 v173, v103
	v_mfma_f32_32x32x16_bf16 v[34:49], v[232:235], v[66:69], v[34:49]
	v_exp_f32_e32 v174, v104
	v_exp_f32_e32 v175, v105
	v_exp_f32_e32 v176, v106
	v_exp_f32_e32 v177, v107
	v_exp_f32_e32 v178, v108
	v_mfma_f32_32x32x16_bf16 v[34:49], v[236:239], v[70:73], v[34:49]
	v_exp_f32_e32 v179, v109
	v_exp_f32_e32 v180, v110
	v_exp_f32_e32 v181, v111
	v_exp_f32_e32 v182, v112
	v_exp_f32_e32 v183, v113
	s_waitcnt lgkmcnt(0)
	s_barrier
; __device__ __forceinline__ void finishSM(f32x16& p0, f32x16& p1, float alpha, float& l_reg, bf16x8& pa0, bf16x8& pa1, bf16x8& pa2, bf16x8& pa3) {
; #pragma unroll
;     for (int r = 0; r < 16; ++r) p1[r] = EXP_PROBE ? fmaf(p1[r], 0.001f, 1.f) : __builtin_amdgcn_exp2f(p1[r]);
;     float ps = 0.f;
; #pragma unroll
;     for (int r = 0; r < 16; ++r) ps += p0[r];
; #pragma unroll
;     for (int r = 0; r < 16; ++r) ps += p1[r];
;     { auto rr = __builtin_amdgcn_permlane32_swap(__float_as_uint(ps), __float_as_uint(ps), false, false);
;       ps = __uint_as_float(rr[0]) + __uint_as_float(rr[1]); }
;     l_reg = l_reg * alpha + ps;
;     ATT_PKN(p0, 0, pa0); ATT_PKN(p0, 8, pa1); ATT_PKN(p1, 0, pa2); ATT_PKN(p1, 8, pa3);
; }
; template <int DQK> __device__ __forceinline__ void qkt(f32x16& p0, f32x16& p1, const LAS char* buf, const bf16x8* qr, int r32, int hi, const f32x16& negm) {
; #pragma unroll
;     for (int d0 = 0; d0 < 4; ++d0) { const int ch = d0 * 2 + hi;
;         const bf16x8 b0 = *(const LAS bf16x8*)(buf + B_KN + swz64(r32, ch));
;         const bf16x8 b1 = *(const LAS bf16x8*)(buf + B_KN + swz64(32 + r32, ch));
;         p0 = __builtin_amdgcn_mfma_f32_32x32x16_bf16(b0, qr[d0], d0 == 0 ? negm : p0, 0, 0, 0);
;         p1 = __builtin_amdgcn_mfma_f32_32x32x16_bf16(b1, qr[d0], d0 == 0 ? negm : p1, 0, 0, 0); }
;     if constexpr (DQK == 96) {
; #pragma unroll
;         for (int d0 = 0; d0 < 2; ++d0) { const int ch = d0 * 2 + hi;
;             const bf16x8 b0 = *(const LAS bf16x8*)(buf + B_KR + swz32(r32, ch));
;             const bf16x8 b1 = *(const LAS bf16x8*)(buf + B_KR + swz32(32 + r32, ch));
;             p0 = __builtin_amdgcn_mfma_f32_32x32x16_bf16(b0, qr[4 + d0], p0, 0, 0, 0);
;             p1 = __builtin_amdgcn_mfma_f32_32x32x16_bf16(b1, qr[4 + d0], p1, 0, 0, 0); }
;     }
; }
; template <int D0> __device__ __forceinline__ void pv_one(f32x16& od, unsigned vb, bf16x8 pa0, bf16x8 pa1, bf16x8 pa2, bf16x8 pa3) {
;     const s16x4 l0 = tr_read<v_rd_off(D0, 0, 0)>(vb), h0 = tr_read<v_rd_off(D0, 0, 1)>(vb), l1 = tr_read<v_rd_off(D0, 1, 0)>(vb), h1 = tr_read<v_rd_off(D0, 1, 1)>(vb);
;     const s16x4 l2 = tr_read<v_rd_off(D0, 2, 0)>(vb), h2 = tr_read<v_rd_off(D0, 2, 1)>(vb), l3 = tr_read<v_rd_off(D0, 3, 0)>(vb), h3 = tr_read<v_rd_off(D0, 3, 1)>(vb);
;     asm volatile("s_waitcnt lgkmcnt(0)" ::: "memory"); SBAR();
	v_add_u32_e32 v252, s10, v201
	v_add_u32_e32 v228, v252, v209
	ds_read_b128 v[224:227], v228
	ds_read_b128 v[228:231], v228 offset:4096
	v_add_u32_e32 v236, v252, v210
	ds_read_b128 v[232:235], v236
	ds_read_b128 v[236:239], v236 offset:4096
	v_add_u32_e32 v244, v252, v211
	ds_read_b128 v[240:243], v244
	ds_read_b128 v[244:247], v244 offset:4096
	v_add_u32_e32 v253, v252, v212
	ds_read_b128 v[248:251], v253
	v_exp_f32_e32 v82, v82
	v_exp_f32_e32 v83, v83
	v_exp_f32_e32 v84, v84
	v_exp_f32_e32 v85, v85
	v_exp_f32_e32 v86, v86
	v_exp_f32_e32 v87, v87
	v_exp_f32_e32 v88, v88
	v_exp_f32_e32 v89, v89
	s_waitcnt lgkmcnt(6)
	v_mfma_f32_32x32x16_bf16 v[98:113], v[224:227], v[114:117], v[18:33]
	ds_read_b128 v[224:227], v253 offset:4096
	v_exp_f32_e32 v90, v90
	v_exp_f32_e32 v91, v91
	v_exp_f32_e32 v92, v92
	v_cvt_pk_bf16_f32 v156, v168, v169
	v_cvt_pk_bf16_f32 v157, v170, v171
	v_add_f32_e32 v164, 0, v168
	v_add_f32_e32 v164, v169, v164
	v_add_f32_e32 v164, v170, v164
	s_waitcnt lgkmcnt(6)
	v_mfma_f32_32x32x16_bf16 v[66:81], v[228:231], v[114:117], v[18:33]
	v_exp_f32_e32 v93, v93
	v_exp_f32_e32 v94, v94
	v_exp_f32_e32 v95, v95
	v_cvt_pk_bf16_f32 v158, v172, v173
	v_cvt_pk_bf16_f32 v159, v174, v175
	v_add_f32_e32 v164, v171, v164
	v_add_f32_e32 v164, v172, v164
	v_add_f32_e32 v164, v173, v164
	s_waitcnt lgkmcnt(5)
	v_mfma_f32_32x32x16_bf16 v[98:113], v[232:235], v[12:15], v[98:113]
	v_exp_f32_e32 v96, v96
	v_exp_f32_e32 v97, v97
	v_cvt_pk_bf16_f32 v160, v176, v177
	v_cvt_pk_bf16_f32 v161, v178, v179
	v_cvt_pk_bf16_f32 v162, v180, v181
	v_cvt_pk_bf16_f32 v163, v182, v183
	v_add_f32_e32 v164, v174, v164
	v_add_f32_e32 v164, v175, v164
	v_add_f32_e32 v164, v176, v164
	s_waitcnt lgkmcnt(4)
	v_mfma_f32_32x32x16_bf16 v[66:81], v[236:239], v[12:15], v[66:81]
	v_add_f32_e32 v164, v177, v164
	v_add_f32_e32 v164, v178, v164
	v_add_f32_e32 v164, v179, v164
	v_add_f32_e32 v164, v180, v164
	v_add_f32_e32 v164, v181, v164
	v_add_f32_e32 v164, v182, v164
	v_add_f32_e32 v164, v183, v164
	s_waitcnt lgkmcnt(3)
	v_mfma_f32_32x32x16_bf16 v[98:113], v[240:243], v[8:11], v[98:113]
	v_add_u32_e32 v253, s1, v213
	ds_read_b64_tr_b16 v[168:169], v253 offset:0
	ds_read_b64_tr_b16 v[170:171], v253 offset:1024
	ds_read_b64_tr_b16 v[172:173], v253 offset:2048
	ds_read_b64_tr_b16 v[174:175], v253 offset:3072
	v_add_f32_e32 v164, v82, v164
	v_add_f32_e32 v164, v83, v164
	v_add_f32_e32 v164, v84, v164
	v_add_f32_e32 v164, v85, v164
	s_waitcnt lgkmcnt(6)
	v_mfma_f32_32x32x16_bf16 v[66:81], v[244:247], v[8:11], v[66:81]
	ds_read_b64_tr_b16 v[176:177], v253 offset:4096
	ds_read_b64_tr_b16 v[178:179], v253 offset:5120
	ds_read_b64_tr_b16 v[180:181], v253 offset:6144
	ds_read_b64_tr_b16 v[182:183], v253 offset:7168
	v_add_f32_e32 v164, v86, v164
	v_add_f32_e32 v164, v87, v164
	v_add_f32_e32 v164, v88, v164
	v_add_f32_e32 v164, v89, v164
	s_waitcnt lgkmcnt(9)
	v_mfma_f32_32x32x16_bf16 v[98:113], v[248:251], v[4:7], v[98:113]
	v_add_f32_e32 v164, v90, v164
	v_add_f32_e32 v164, v91, v164
	v_add_f32_e32 v164, v92, v164
	v_add_f32_e32 v164, v93, v164
	ds_read_b64_tr_b16 v[228:229], v253 offset:2560
	ds_read_b64_tr_b16 v[230:231], v253 offset:3584
	ds_read_b64_tr_b16 v[232:233], v253 offset:4608
	s_waitcnt lgkmcnt(11)
	v_mfma_f32_32x32x16_bf16 v[66:81], v[224:227], v[4:7], v[66:81]
	ds_read_b64_tr_b16 v[234:235], v253 offset:5632
	ds_read_b64_tr_b16 v[236:237], v253 offset:6656
	ds_read_b64_tr_b16 v[238:239], v253 offset:7680
	ds_read_b64_tr_b16 v[224:225], v253 offset:512
	ds_read_b64_tr_b16 v[226:227], v253 offset:1536
	s_waitcnt lgkmcnt(8)
	v_mfma_f32_32x32x16_bf16 v[50:65], v[168:171], v[156:159], v[50:65]
	v_add_f32_e32 v164, v94, v164
	v_add_f32_e32 v164, v95, v164
	v_add_f32_e32 v164, v96, v164
	v_add_f32_e32 v164, v97, v164
	v_mov_b32_e32 v165, v164
	v_mfma_f32_32x32x16_bf16 v[50:65], v[172:175], v[160:163], v[50:65]
	v_cvt_pk_bf16_f32 v82, v82, v83
	v_cvt_pk_bf16_f32 v83, v84, v85
	v_cvt_pk_bf16_f32 v84, v86, v87
	v_cvt_pk_bf16_f32 v85, v88, v89
	v_cvt_pk_bf16_f32 v86, v90, v91
	v_cvt_pk_bf16_f32 v87, v92, v93
	v_cvt_pk_bf16_f32 v88, v94, v95
	v_cvt_pk_bf16_f32 v89, v96, v97
	v_permlane32_swap_b32_e32 v164, v165
	v_mfma_f32_32x32x16_bf16 v[50:65], v[176:179], v[82:85], v[50:65]
	v_mfma_f32_32x32x16_bf16 v[50:65], v[180:183], v[86:89], v[50:65]
	s_cmp_ge_u32 s13, s30
	s_cbranch_scc1 .Lgqa_b_noload
	s_cmp_lt_u32 s13, s31
	s_cselect_b32 s9, 0, s31
	s_cselect_b32 s35, s12, s29
	s_lshl_b32 s9, s9, 6
	s_sub_i32 s9, s35, s9
	v_add_u32_e32 v118, s9, v137
	v_ashrrev_i32_e32 v119, 31, v118
	v_lshlrev_b64 v[118:119], 8, v[118:119]
	v_lshl_add_u64 v[120:121], v[16:17], 0, v[118:119]
	v_lshl_add_u64 v[122:123], v[134:135], 0, v[118:119]
	global_load_dwordx4 v[118:121], v[120:121], off
	s_nop 0
	global_load_dwordx4 v[122:125], v[122:123], off
